# P0 S5 unit: D-skip entry preloaded with the other operands (one more exposed round trip removed)
# baseline (speedup 1.0000x reference)
; DI const float* inp(kptr_t k, int i) { return (const float*)k[i]; }
; DI double exp_d(double x) {
;     const double kf = __builtin_rint(x * 1.4426950408889634); const double r = x - kf * 0.6931471805599453094;
;     double t = 1.0, s = 1.0;
; #pragma unroll
;     for (int i = 1; i <= 16; ++i) { t *= r * (1.0 / (double)i); s += t; }
;     const int k = (int)kf;
;     return __builtin_ldexp(s, k);
; }
; DI void p_ssm_unit(Frame& F, int unit) {
;     ...
;     const double dt = exp_d((double)inp(KA, I_LOGDT)[lg]);
;     for (int i = F.tid; i < 33 * 64; i += 512) { const int tau = i >> 6, p = i & 63;
;         const double lre = fmin((double)inp(KA, I_ARE)[lg * SP + p], -1e-4), lim = (double)inp(KA, I_AIM)[lg * SP + p];
;         const double mag = exp_d(lre * dt * (double)tau); double sn, cs; sincos_d(lim * dt * (double)tau, sn, cs);
;         Lp[i * 2] = mag * cs; Lp[i * 2 + 1] = mag * sn; }
;     __syncthreads();
;     for (int i = F.tid; i < SP * SG; i += 512) { const int p = i >> 4, cc = i & 15;
;         const double lre = fmin((double)inp(KA, I_ARE)[lg * SP + p], -1e-4), lim = (double)inp(KA, I_AIM)[lg * SP + p];
;         const double nre = Lp[(64 + p) * 2] - 1.0, nim = Lp[(64 + p) * 2 + 1], den = lre * lre + lim * lim;
;         const double zre = (nre * lre + nim * lim) / den, zim = (nim * lre - nre * lim) / den;
;         const double br = (double)inp(KA, I_BRE)[((size_t)lg * SP + p) * SG + cc], bi = (double)inp(KA, I_BIM)[((size_t)lg * SP + p) * SG + cc];
;         Bb[i * 2] = (float)(zre * br - zim * bi); Bb[i * 2 + 1] = (float)(zre * bi + zim * br); }
;     for (int i = F.tid; i < SG * SP; i += 512) { Cc[i * 2] = inp(KA, I_CRE)[(size_t)lg * SG * SP + i]; Cc[i * 2 + 1] = inp(KA, I_CIM)[(size_t)lg * SG * SP + i]; }
.LBB0_17:
	s_and_b64 vcc, exec, s[4:5]
	s_cbranch_vccz .LBB0_76
	s_mov_b32 s97, s12
	s_mov_b32 s4, -1
	s_lshl_b32 s44, s97, 6
	v_mbcnt_lo_u32_b32 v0, s4, 0
	v_mbcnt_hi_u32_b32 v20, s4, v0
	v_readlane_b32 s4, v253, 29
	v_readlane_b32 s5, v253, 30
	v_add_u32_e32 v10, s44, v20
	s_mov_b32 s14, 0x6dc9c883
	v_readlane_b32 s90, v253, 6
	s_movk_i32 s4, 0x840
	s_mov_b32 s15, 0x3fc45f30
	v_readlane_b32 s91, v253, 7
	s_ashr_i32 s89, s88, 31
	v_cmp_gt_i32_e64 s[4:5], s4, v10
	s_and_saveexec_b64 s[6:7], s[4:5]
	s_cbranch_execz .LBB0_21
	s_load_dwordx2 s[8:9], s[90:91], 0x60
	s_lshl_b64 s[10:11], s[88:89], 2
	s_mov_b32 s70, s18
	s_mov_b32 s72, s16
	s_mov_b32 s74, s20
	s_waitcnt lgkmcnt(0)
	s_add_u32 s8, s8, s10
	s_addc_u32 s9, s9, s11
	global_load_dword v4, v9, s[8:9]
	s_load_dwordx4 s[8:11], s[90:91], 0x50
	s_lshl_b32 s12, s88, 6
	v_and_or_b32 v0, v20, 63, s12
	v_ashrrev_i32_e32 v1, 31, v0
	v_lshlrev_b64 v[0:1], 2, v[0:1]
	s_waitcnt lgkmcnt(0)
	v_lshl_add_u64 v[2:3], s[8:9], 0, v[0:1]
	v_lshl_add_u64 v[0:1], s[10:11], 0, v[0:1]
	global_load_dword v11, v[2:3], off
	global_load_dword v21, v[0:1], off
	v_lshrrev_b32_e32 v252, 4, v10
	v_lshlrev_b32_e32 v252, 2, v252
	s_lshl_b32 s98, s88, 8
	s_add_u32 s8, s8, s98
	s_addc_u32 s9, s9, 0
	s_add_u32 s10, s10, s98
	s_addc_u32 s11, s11, 0
	global_load_dword v240, v252, s[8:9]
	global_load_dword v241, v252, s[10:11]
	global_load_dword v242, v252, s[8:9] offset:128
	global_load_dword v243, v252, s[10:11] offset:128
	s_load_dwordx4 s[8:11], s[90:91], 0x68
	v_lshlrev_b32_e32 v252, 2, v10
	s_lshl_b32 s98, s88, 12
	s_waitcnt lgkmcnt(0)
	s_add_u32 s8, s8, s98
	s_addc_u32 s9, s9, 0
	s_add_u32 s10, s10, s98
	s_addc_u32 s11, s11, 0
	global_load_dword v244, v252, s[10:11]
	global_load_dword v245, v252, s[8:9]
	global_load_dword v246, v252, s[10:11] offset:2048
	global_load_dword v247, v252, s[8:9] offset:2048
	s_load_dwordx4 s[8:11], s[90:91], 0x78
	s_waitcnt lgkmcnt(0)
	s_add_u32 s8, s8, s98
	s_addc_u32 s9, s9, 0
	s_add_u32 s10, s10, s98
	s_addc_u32 s11, s11, 0
	global_load_dword v248, v252, s[8:9]
	global_load_dword v249, v252, s[10:11]
	global_load_dword v250, v252, s[8:9] offset:2048
	global_load_dword v251, v252, s[10:11] offset:2048
	s_load_dwordx2 s[8:9], s[90:91], 0x88
	v_and_b32_e32 v252, 15, v20
	v_lshlrev_b32_e32 v252, 2, v252
	s_lshl_b32 s98, s88, 6
	s_waitcnt lgkmcnt(0)
	s_add_u32 s8, s8, s98
	s_addc_u32 s9, s9, 0
	global_load_dword v252, v252, s[8:9]
	s_mov_b32 s76, s22
	s_mov_b32 s78, s18
	s_mov_b32 s80, s16
	s_mov_b32 s82, s20
	s_mov_b32 s84, s28
	s_lshl_b32 s10, s97, 10
	s_add_i32 s10, s10, 0
	s_mov_b64 s[8:9], 0
	v_lshl_add_u32 v8, v20, 4, s10
	s_waitcnt vmcnt(15)
	v_cvt_f64_f32_e32 v[0:1], v4
	v_mul_f64 v[2:3], v[0:1], s[0:1]
	v_rndne_f64_e32 v[2:3], v[2:3]
	v_fmac_f64_e32 v[0:1], s[2:3], v[2:3]
	v_cvt_i32_f64_e32 v24, v[2:3]
	v_add_f64 v[2:3], v[0:1], 1.0
	v_mul_f64 v[4:5], v[0:1], 0.5
	v_mul_f64 v[6:7], v[0:1], s[16:17]
	v_mul_f64 v[46:47], v[0:1], v[4:5]
	v_fmac_f64_e32 v[2:3], v[0:1], v[4:5]
	v_ldexp_f64 v[12:13], v[0:1], -2
	v_mul_f64 v[4:5], v[6:7], v[46:47]
	v_fmac_f64_e32 v[2:3], v[6:7], v[46:47]
	v_mul_f64 v[14:15], v[0:1], s[70:71]
	v_mul_f64 v[6:7], v[12:13], v[4:5]
	v_fmac_f64_e32 v[2:3], v[12:13], v[4:5]
	v_mul_f64 v[16:17], v[0:1], s[72:73]
	v_mul_f64 v[4:5], v[14:15], v[6:7]
	v_fmac_f64_e32 v[2:3], v[14:15], v[6:7]
	v_mul_f64 v[18:19], v[0:1], s[74:75]
	v_mul_f64 v[6:7], v[16:17], v[4:5]
	v_fmac_f64_e32 v[2:3], v[16:17], v[4:5]
	v_ldexp_f64 v[22:23], v[0:1], -3
	v_mul_f64 v[4:5], v[18:19], v[6:7]
	v_fmac_f64_e32 v[2:3], v[18:19], v[6:7]
	v_mul_f64 v[26:27], v[0:1], s[76:77]
	v_mul_f64 v[6:7], v[22:23], v[4:5]
	v_fmac_f64_e32 v[2:3], v[22:23], v[4:5]
	v_mul_f64 v[28:29], v[0:1], s[78:79]
	v_mul_f64 v[4:5], v[26:27], v[6:7]
	v_fmac_f64_e32 v[2:3], v[26:27], v[6:7]
	v_mul_f64 v[30:31], v[0:1], s[24:25]
	v_mul_f64 v[6:7], v[28:29], v[4:5]
	v_fmac_f64_e32 v[2:3], v[28:29], v[4:5]
	v_mul_f64 v[32:33], v[0:1], s[80:81]
	v_mul_f64 v[4:5], v[30:31], v[6:7]
	v_fmac_f64_e32 v[2:3], v[30:31], v[6:7]
	v_mul_f64 v[34:35], v[0:1], s[26:27]
	v_mul_f64 v[6:7], v[32:33], v[4:5]
	v_fmac_f64_e32 v[2:3], v[32:33], v[4:5]
	v_mul_f64 v[36:37], v[0:1], s[82:83]
	v_mul_f64 v[4:5], v[34:35], v[6:7]
	v_fmac_f64_e32 v[2:3], v[34:35], v[6:7]
	v_mul_f64 v[38:39], v[0:1], s[84:85]
	v_mul_f64 v[6:7], v[36:37], v[4:5]
	v_fmac_f64_e32 v[2:3], v[36:37], v[4:5]
	v_ldexp_f64 v[40:41], v[0:1], -4
	v_mul_f64 v[4:5], v[38:39], v[6:7]
	v_fmac_f64_e32 v[2:3], v[38:39], v[6:7]
	s_waitcnt vmcnt(14)
	v_cvt_f64_f32_e32 v[42:43], v11
	v_fmac_f64_e32 v[2:3], v[40:41], v[4:5]
	s_waitcnt vmcnt(13)
	v_cvt_f64_f32_e32 v[44:45], v21
	v_min_f64 v[0:1], v[42:43], s[30:31]
	v_ldexp_f64 v[2:3], v[2:3], v24
	v_mul_f64 v[0:1], v[0:1], v[2:3]
	v_mul_f64 v[2:3], v[2:3], v[44:45]
	v_mov_b32_e32 v11, v10

; DI const float* inp(kptr_t k, int i) { return (const float*)k[i]; }
; DI void p_ssm_unit(Frame& F, int unit) {
;     ...
;     { const int pair = F.tid & 255, cc = pair >> 4, c2 = pair & 15, t0 = (F.tid >> 8) * 16; float acc[16];
; #pragma unroll
;       for (int q = 0; q < 16; ++q) acc[q] = 0.f;
;       for (int p = 0; p < SP; ++p) { const float cr = Cc[(cc * 64 + p) * 2], ci = Cc[(cc * 64 + p) * 2 + 1], br = Bb[(p * 16 + c2) * 2], bi = Bb[(p * 16 + c2) * 2 + 1];
;           const float gr = cr * br - ci * bi, gi = cr * bi + ci * br;
; #pragma unroll
;           for (int q = 0; q < 16; ++q) { const f32x2 lv = Lf[(t0 + q) * 64 + p]; acc[q] += gr * lv[0] - gi * lv[1]; } }
;       if (t0 == 0 && cc == c2) acc[0] += inp(KA, I_DSKIP)[l * SW + g * 16 + cc];
.LBB0_42:
	v_add_u32_e32 v90, s4, v26
	v_add_u32_e32 v94, s4, v24
	v_add_u32_e32 v34, 0x18600, v90
	v_add_u32_e32 v38, 0x18800, v90
	v_add_u32_e32 v42, 0x18a00, v90
	v_add_u32_e32 v46, 0x18c00, v90
	v_add_u32_e32 v50, 0x18e00, v90
	v_add_u32_e32 v54, 0x19000, v90
	v_add_u32_e32 v58, 0x19200, v90
	v_add_u32_e32 v62, 0x19400, v90
	v_add_u32_e32 v66, 0x19600, v90
	v_add_u32_e32 v70, 0x19800, v90
	v_add_u32_e32 v74, 0x19a00, v90
	v_add_u32_e32 v78, 0x19c00, v90
	v_add_u32_e32 v82, 0x19e00, v90
	v_add_u32_e32 v86, 0x1a000, v90
	v_add_u32_e32 v90, 0x1a200, v90
	v_add_u32_e32 v94, 0x18600, v94
	v_add_u32_e32 v29, s4, v27
	ds_read2_b64 v[30:33], v28 offset1:16
	ds_read_b128 v[34:37], v34
	ds_read_b128 v[38:41], v38
	ds_read_b128 v[42:45], v42
	ds_read_b128 v[46:49], v46
	ds_read_b128 v[50:53], v50
	ds_read_b128 v[54:57], v54
	ds_read_b128 v[58:61], v58
	ds_read_b128 v[62:65], v62
	ds_read_b128 v[66:69], v66
	ds_read_b128 v[70:73], v70
	ds_read_b128 v[74:77], v74
	ds_read_b128 v[78:81], v78
	ds_read_b128 v[82:85], v82
	ds_read_b128 v[86:89], v86
	ds_read_b128 v[90:93], v90
	ds_read_b128 v[94:97], v94
	ds_read_b128 v[98:101], v29 offset:512
	s_add_i32 s4, s4, 16
	v_add_u32_e32 v28, 0x100, v28
	s_cmp_eq_u32 s4, 0
	s_waitcnt lgkmcnt(0)
	v_pk_mul_f32 v[102:103], v[98:99], v[30:31] op_sel:[1,1] op_sel_hi:[0,1]
	v_pk_fma_f32 v[104:105], v[98:99], v[30:31], v[102:103] op_sel_hi:[1,0,1] neg_lo:[0,0,1] neg_hi:[0,0,1]
	v_pk_fma_f32 v[30:31], v[98:99], v[30:31], v[102:103] op_sel_hi:[1,0,1]
	v_mov_b32_e32 v103, v38
	v_mov_b32_e32 v38, v35
	v_mov_b32_e32 v102, v34
	v_pk_mul_f32 v[34:35], v[30:31], v[38:39] op_sel:[1,0]
	v_mov_b32_e32 v99, v31
	v_pk_fma_f32 v[34:35], v[104:105], v[102:103], v[34:35] op_sel_hi:[0,1,1] neg_lo:[0,0,1] neg_hi:[0,0,1]
	v_pk_add_f32 v[2:3], v[2:3], v[34:35]
	v_mov_b32_e32 v35, v46
	v_mov_b32_e32 v46, v43
	v_mov_b32_e32 v34, v42
	v_pk_mul_f32 v[38:39], v[30:31], v[46:47] op_sel:[1,0]
	v_mov_b32_e32 v98, v104
	v_pk_fma_f32 v[34:35], v[104:105], v[34:35], v[38:39] op_sel_hi:[0,1,1] neg_lo:[0,0,1] neg_hi:[0,0,1]
	v_pk_add_f32 v[4:5], v[4:5], v[34:35]
	v_mov_b32_e32 v35, v54
	v_mov_b32_e32 v54, v51
	v_mov_b32_e32 v34, v50
	v_pk_mul_f32 v[38:39], v[30:31], v[54:55] op_sel:[1,0]
	s_nop 0
	v_pk_fma_f32 v[34:35], v[104:105], v[34:35], v[38:39] op_sel_hi:[0,1,1] neg_lo:[0,0,1] neg_hi:[0,0,1]
	v_pk_add_f32 v[6:7], v[6:7], v[34:35]
	v_mov_b32_e32 v35, v62
	v_mov_b32_e32 v62, v59
	v_mov_b32_e32 v34, v58
	v_pk_mul_f32 v[38:39], v[30:31], v[62:63] op_sel:[1,0]
	s_nop 0
	v_pk_fma_f32 v[34:35], v[104:105], v[34:35], v[38:39] op_sel_hi:[0,1,1] neg_lo:[0,0,1] neg_hi:[0,0,1]
	v_pk_add_f32 v[12:13], v[12:13], v[34:35]
	v_mov_b32_e32 v35, v70
	v_mov_b32_e32 v70, v67
	v_mov_b32_e32 v34, v66
	v_pk_mul_f32 v[38:39], v[30:31], v[70:71] op_sel:[1,0]
	s_nop 0
	v_pk_fma_f32 v[34:35], v[104:105], v[34:35], v[38:39] op_sel_hi:[0,1,1] neg_lo:[0,0,1] neg_hi:[0,0,1]
	v_pk_add_f32 v[14:15], v[14:15], v[34:35]
	v_mov_b32_e32 v35, v78
	v_mov_b32_e32 v78, v75
	v_mov_b32_e32 v34, v74
	v_pk_mul_f32 v[38:39], v[30:31], v[78:79] op_sel:[1,0]
	s_nop 0
	v_pk_fma_f32 v[34:35], v[104:105], v[34:35], v[38:39] op_sel_hi:[0,1,1] neg_lo:[0,0,1] neg_hi:[0,0,1]
	v_pk_add_f32 v[16:17], v[16:17], v[34:35]
	v_mov_b32_e32 v35, v86
	v_mov_b32_e32 v86, v83
	v_mov_b32_e32 v34, v82
	v_pk_mul_f32 v[30:31], v[30:31], v[86:87] op_sel:[1,0]
	s_nop 0
	v_pk_fma_f32 v[30:31], v[104:105], v[34:35], v[30:31] op_sel_hi:[0,1,1] neg_lo:[0,0,1] neg_hi:[0,0,1]
	v_pk_add_f32 v[18:19], v[18:19], v[30:31]
	v_pk_mul_f32 v[30:31], v[98:99], v[90:91]
	v_pk_mul_f32 v[34:35], v[98:99], v[94:95]
	v_mov_b32_e32 v38, v30
	v_mov_b32_e32 v39, v34
	v_mov_b32_e32 v34, v31
	v_pk_add_f32 v[30:31], v[38:39], v[34:35] neg_lo:[0,1] neg_hi:[0,1]
	v_mov_b32_e32 v39, v40
	v_pk_add_f32 v[0:1], v[0:1], v[30:31]
	v_pk_mul_f32 v[30:31], v[100:101], v[32:33] op_sel:[1,1] op_sel_hi:[0,1]
	v_pk_fma_f32 v[34:35], v[100:101], v[32:33], v[30:31] op_sel_hi:[1,0,1] neg_lo:[0,0,1] neg_hi:[0,0,1]
	v_pk_fma_f32 v[30:31], v[100:101], v[32:33], v[30:31] op_sel_hi:[1,0,1]
	v_mov_b32_e32 v40, v37
	v_mov_b32_e32 v38, v36
	v_pk_mul_f32 v[36:37], v[30:31], v[40:41] op_sel:[1,0]
	v_mov_b32_e32 v33, v31
	v_pk_fma_f32 v[36:37], v[34:35], v[38:39], v[36:37] op_sel_hi:[0,1,1] neg_lo:[0,0,1] neg_hi:[0,0,1]
	v_pk_add_f32 v[2:3], v[2:3], v[36:37]
	v_mov_b32_e32 v37, v48
	v_mov_b32_e32 v48, v45
	v_mov_b32_e32 v36, v44
	v_pk_mul_f32 v[38:39], v[30:31], v[48:49] op_sel:[1,0]
	v_mov_b32_e32 v32, v34
	v_pk_fma_f32 v[36:37], v[34:35], v[36:37], v[38:39] op_sel_hi:[0,1,1] neg_lo:[0,0,1] neg_hi:[0,0,1]
	v_pk_add_f32 v[4:5], v[4:5], v[36:37]
	v_mov_b32_e32 v37, v56
	v_mov_b32_e32 v56, v53
	v_mov_b32_e32 v36, v52
	v_pk_mul_f32 v[38:39], v[30:31], v[56:57] op_sel:[1,0]
	s_nop 0
	v_pk_fma_f32 v[36:37], v[34:35], v[36:37], v[38:39] op_sel_hi:[0,1,1] neg_lo:[0,0,1] neg_hi:[0,0,1]
	v_pk_add_f32 v[6:7], v[6:7], v[36:37]
	v_mov_b32_e32 v37, v64
	v_mov_b32_e32 v64, v61
	v_mov_b32_e32 v36, v60
	v_pk_mul_f32 v[38:39], v[30:31], v[64:65] op_sel:[1,0]
	s_nop 0
	v_pk_fma_f32 v[36:37], v[34:35], v[36:37], v[38:39] op_sel_hi:[0,1,1] neg_lo:[0,0,1] neg_hi:[0,0,1]
	v_pk_add_f32 v[12:13], v[12:13], v[36:37]
	v_mov_b32_e32 v37, v72
	v_mov_b32_e32 v72, v69
	v_mov_b32_e32 v36, v68
	v_pk_mul_f32 v[38:39], v[30:31], v[72:73] op_sel:[1,0]
	s_nop 0
	v_pk_fma_f32 v[36:37], v[34:35], v[36:37], v[38:39] op_sel_hi:[0,1,1] neg_lo:[0,0,1] neg_hi:[0,0,1]
	v_pk_add_f32 v[14:15], v[14:15], v[36:37]
	v_mov_b32_e32 v37, v80
	v_mov_b32_e32 v80, v77
	v_mov_b32_e32 v36, v76
	v_pk_mul_f32 v[38:39], v[30:31], v[80:81] op_sel:[1,0]
	s_nop 0
	v_pk_fma_f32 v[36:37], v[34:35], v[36:37], v[38:39] op_sel_hi:[0,1,1] neg_lo:[0,0,1] neg_hi:[0,0,1]
	v_pk_add_f32 v[16:17], v[16:17], v[36:37]
	v_mov_b32_e32 v37, v88
	v_mov_b32_e32 v88, v85
	v_mov_b32_e32 v36, v84
	v_pk_mul_f32 v[30:31], v[30:31], v[88:89] op_sel:[1,0]
	s_nop 0
	v_pk_fma_f32 v[30:31], v[34:35], v[36:37], v[30:31] op_sel_hi:[0,1,1] neg_lo:[0,0,1] neg_hi:[0,0,1]
	v_pk_add_f32 v[18:19], v[18:19], v[30:31]
	v_pk_mul_f32 v[30:31], v[32:33], v[92:93]
	v_pk_mul_f32 v[32:33], v[32:33], v[96:97]
	v_mov_b32_e32 v34, v30
	v_mov_b32_e32 v35, v32
	v_mov_b32_e32 v32, v31
	v_pk_add_f32 v[30:31], v[34:35], v[32:33] neg_lo:[0,1] neg_hi:[0,1]
	s_nop 0
	v_pk_add_f32 v[0:1], v[0:1], v[30:31]
	s_cbranch_scc0 .LBB0_42
	v_cmp_eq_u32_e32 vcc, 0, v22
	v_cmp_eq_u32_e64 s[4:5], v11, v23
	s_and_b64 s[6:7], vcc, s[4:5]
	s_and_saveexec_b64 s[4:5], s[6:7]
	s_cbranch_execz .LBB0_45
	v_add_f32_e32 v2, v2, v252
